# NA attention tile loops: 4 K fragments / 5 V fragments prefetched from LDS with counted lgkmcnt waits (as in the MLA loops)
# baseline (speedup 1.0000x reference)
.LBB0_717:
	s_andn2_b64 vcc, exec, s[48:49]
	s_cbranch_vccnz .LBB0_757
	s_bitcmp1_b32 s86, 0
	s_cselect_b32 s48, 0x8c00, 0
	s_add_i32 s86, s48, 0
	v_add3_u32 v2, s86, v194, v168
	ds_read_b128 v[4:7], v2
	ds_read_b128 v[8:11], v2 offset:32
	ds_read_b128 v[248:251], v2 offset:64
	ds_read_b128 v[252:255], v2 offset:96
	s_mov_b64 s[48:49], -1
	s_andn2_b64 vcc, exec, s[46:47]
	s_waitcnt lgkmcnt(3)
	v_mfma_f32_32x32x16_bf16 v[100:115], v[4:7], v[116:119], 0
	ds_read_b128 v[4:7], v2 offset:128
	s_waitcnt lgkmcnt(3)
	v_mfma_f32_32x32x16_bf16 v[100:115], v[8:11], v[120:123], v[100:115]
	ds_read_b128 v[8:11], v2 offset:160
	s_waitcnt lgkmcnt(3)
	v_mfma_f32_32x32x16_bf16 v[100:115], v[248:251], v[128:131], v[100:115]
	ds_read_b128 v[248:251], v2 offset:192
	s_waitcnt lgkmcnt(3)
	v_mfma_f32_32x32x16_bf16 v[100:115], v[252:255], v[136:139], v[100:115]
	ds_read_b128 v[252:255], v2 offset:224
	v_max_f32_e32 v2, v83, v83
	s_waitcnt lgkmcnt(3)
	v_mfma_f32_32x32x16_bf16 v[100:115], v[4:7], v[140:143], v[100:115]
	s_waitcnt lgkmcnt(2)
	v_mfma_f32_32x32x16_bf16 v[100:115], v[8:11], v[144:147], v[100:115]
	s_waitcnt lgkmcnt(1)
	v_mfma_f32_32x32x16_bf16 v[100:115], v[248:251], v[148:151], v[100:115]
	s_waitcnt lgkmcnt(0)
	v_mfma_f32_32x32x16_bf16 v[100:115], v[252:255], v[152:155], v[100:115]
	s_cbranch_vccnz .LBB0_720
	s_nop 10
	v_max3_f32 v4, v100, s58, v101
	v_max3_f32 v4, v4, v102, v103
	v_max3_f32 v4, v4, v104, v105
	v_max3_f32 v4, v4, v106, v107
	v_max3_f32 v4, v4, v108, v109
	v_max3_f32 v4, v4, v110, v111
	v_max3_f32 v4, v4, v112, v113
	v_max3_f32 v4, v4, v114, v115
	v_mov_b32_e32 v5, v4
	s_nop 1
	v_permlane32_swap_b32_e32 v4, v5
	v_mul_f32_e32 v4, 0x3e0293ee, v4
	v_max_f32_e32 v4, v2, v4
	v_fma_f32 v5, v100, s59, -v4
	v_exp_f32_e32 v84, v5
	v_fma_f32 v5, v101, s59, -v4
	v_exp_f32_e32 v85, v5
	v_fma_f32 v5, v102, s59, -v4
	v_exp_f32_e32 v86, v5
	v_fma_f32 v6, v103, s59, -v4
	v_exp_f32_e32 v87, v6
	v_fma_f32 v6, v104, s59, -v4
	v_add_f32_e32 v5, 0, v84
	v_exp_f32_e32 v88, v6
	v_fma_f32 v6, v105, s59, -v4
	v_add_f32_e32 v5, v85, v5
	v_exp_f32_e32 v89, v6
	v_fma_f32 v6, v106, s59, -v4
	v_add_f32_e32 v5, v86, v5
	v_exp_f32_e32 v90, v6
	v_fma_f32 v6, v107, s59, -v4
	v_add_f32_e32 v5, v87, v5
	v_exp_f32_e32 v91, v6
	v_fma_f32 v6, v108, s59, -v4
	v_add_f32_e32 v5, v88, v5
	v_exp_f32_e32 v92, v6
	v_fma_f32 v6, v109, s59, -v4
	v_add_f32_e32 v5, v89, v5
	v_exp_f32_e32 v93, v6
	v_fma_f32 v6, v110, s59, -v4
	v_add_f32_e32 v5, v90, v5
	v_exp_f32_e32 v94, v6
	v_fma_f32 v6, v111, s59, -v4
	v_add_f32_e32 v5, v91, v5
	v_exp_f32_e32 v95, v6
	v_fma_f32 v6, v112, s59, -v4
	v_add_f32_e32 v5, v92, v5
	v_exp_f32_e32 v96, v6
	v_fma_f32 v6, v113, s59, -v4
	v_add_f32_e32 v5, v93, v5
	v_exp_f32_e32 v97, v6
	v_fma_f32 v6, v114, s59, -v4
	v_add_f32_e32 v5, v94, v5
	v_exp_f32_e32 v98, v6
	v_add_f32_e32 v5, v95, v5
	v_add_f32_e32 v5, v96, v5
	v_add_f32_e32 v5, v97, v5
	v_add_f32_e32 v6, v98, v5
	v_fma_f32 v5, v115, s59, -v4
	s_mov_b64 s[48:49], 0

.LBB0_756:
	v_add_f32_e32 v14, v6, v6
	s_lshl_b32 s46, s55, 1
	v_fmac_f32_e32 v14, v82, v2
	s_add_i32 s46, s46, s86
	v_lshlrev_b32_e32 v2, 1, v180
	v_add3_u32 v2, s46, v195, v2
	v_add_u32_e32 v15, 0x4000, v2
	v_cvt_pk_bf16_f32 v6, v84, v85
	v_cvt_pk_bf16_f32 v7, v86, v87
	v_cvt_pk_bf16_f32 v8, v88, v89
	v_cvt_pk_bf16_f32 v9, v90, v91
	v_cvt_pk_bf16_f32 v92, v92, v93
	v_cvt_pk_bf16_f32 v93, v94, v95
	v_cvt_pk_bf16_f32 v94, v96, v97
	v_cvt_pk_bf16_f32 v95, v98, v5
	v_add_u32_e32 v16, 0x5000, v2
	v_add_u32_e32 v17, 0x6800, v2
	v_add_u32_e32 v2, 0x7800, v2
	v_mov_b32_e32 v82, v14
	ds_read2_b64 v[10:13], v15 offset0:128 offset1:130
	ds_read2_b64 v[248:251], v16 offset0:192 offset1:194
	ds_read2_b64 v[252:255], v17 offset1:2
	ds_read2_b64 v[84:87], v2 offset0:64 offset1:66
	ds_read2_b64 v[88:91], v15 offset0:132 offset1:134
	s_waitcnt lgkmcnt(4)
	v_mfma_f32_32x32x16_bf16 v[66:81], v[10:13], v[6:9], v[66:81]
	ds_read2_b64 v[10:13], v16 offset0:196 offset1:198
	s_waitcnt lgkmcnt(4)
	v_mfma_f32_32x32x16_bf16 v[50:65], v[248:251], v[6:9], v[50:65]
	ds_read2_b64 v[248:251], v17 offset0:4 offset1:6
	s_waitcnt lgkmcnt(4)
	v_mfma_f32_32x32x16_bf16 v[34:49], v[252:255], v[6:9], v[34:49]
	ds_read2_b64 v[252:255], v2 offset0:68 offset1:70
	s_waitcnt lgkmcnt(4)
	v_mfma_f32_32x32x16_bf16 v[18:33], v[84:87], v[6:9], v[18:33]
	s_waitcnt lgkmcnt(3)
	v_mfma_f32_32x32x16_bf16 v[66:81], v[88:91], v[92:95], v[66:81]
	s_waitcnt lgkmcnt(2)
	v_mfma_f32_32x32x16_bf16 v[50:65], v[10:13], v[92:95], v[50:65]
	s_waitcnt lgkmcnt(1)
	v_mfma_f32_32x32x16_bf16 v[34:49], v[248:251], v[92:95], v[34:49]
	s_waitcnt lgkmcnt(0)
	v_mfma_f32_32x32x16_bf16 v[18:33], v[252:255], v[92:95], v[18:33]
	s_andn2_b64 vcc, exec, s[44:45]
	s_cbranch_vccz .LBB0_758
	s_branch .LBB0_759

.LBB0_2900:
	s_andn2_b64 vcc, exec, s[54:55]
	s_cbranch_vccnz .LBB0_2940
	s_bitcmp1_b32 s86, 0
	s_cselect_b32 s54, 0x8c00, 0
	s_add_i32 s86, s54, 0
	v_add3_u32 v2, s86, v197, v170
	ds_read_b128 v[4:7], v2
	ds_read_b128 v[8:11], v2 offset:32
	ds_read_b128 v[248:251], v2 offset:64
	ds_read_b128 v[252:255], v2 offset:96
	s_mov_b64 s[54:55], -1
	s_andn2_b64 vcc, exec, s[50:51]
	s_waitcnt lgkmcnt(3)
	v_mfma_f32_32x32x16_bf16 v[100:115], v[4:7], v[116:119], 0
	ds_read_b128 v[4:7], v2 offset:128
	s_waitcnt lgkmcnt(3)
	v_mfma_f32_32x32x16_bf16 v[100:115], v[8:11], v[120:123], v[100:115]
	ds_read_b128 v[8:11], v2 offset:160
	s_waitcnt lgkmcnt(3)
	v_mfma_f32_32x32x16_bf16 v[100:115], v[248:251], v[128:131], v[100:115]
	ds_read_b128 v[248:251], v2 offset:192
	s_waitcnt lgkmcnt(3)
	v_mfma_f32_32x32x16_bf16 v[100:115], v[252:255], v[136:139], v[100:115]
	ds_read_b128 v[252:255], v2 offset:224
	v_max_f32_e32 v2, v83, v83
	s_waitcnt lgkmcnt(3)
	v_mfma_f32_32x32x16_bf16 v[100:115], v[4:7], v[140:143], v[100:115]
	s_waitcnt lgkmcnt(2)
	v_mfma_f32_32x32x16_bf16 v[100:115], v[8:11], v[144:147], v[100:115]
	s_waitcnt lgkmcnt(1)
	v_mfma_f32_32x32x16_bf16 v[100:115], v[248:251], v[148:151], v[100:115]
	s_waitcnt lgkmcnt(0)
	v_mfma_f32_32x32x16_bf16 v[100:115], v[252:255], v[152:155], v[100:115]
	s_cbranch_vccnz .LBB0_2903
	s_nop 10
	v_max3_f32 v4, v100, s62, v101
	v_max3_f32 v4, v4, v102, v103
	v_max3_f32 v4, v4, v104, v105
	v_max3_f32 v4, v4, v106, v107
	v_max3_f32 v4, v4, v108, v109
	v_max3_f32 v4, v4, v110, v111
	v_max3_f32 v4, v4, v112, v113
	v_max3_f32 v4, v4, v114, v115
	v_mov_b32_e32 v5, v4
	s_nop 1
	v_permlane32_swap_b32_e32 v4, v5
	v_mul_f32_e32 v4, 0x3e0293ee, v4
	v_max_f32_e32 v4, v2, v4
	v_fma_f32 v5, v100, s63, -v4
	v_exp_f32_e32 v84, v5
	v_fma_f32 v5, v101, s63, -v4
	v_exp_f32_e32 v85, v5
	v_fma_f32 v5, v102, s63, -v4
	v_exp_f32_e32 v86, v5
	v_fma_f32 v6, v103, s63, -v4
	v_exp_f32_e32 v87, v6
	v_fma_f32 v6, v104, s63, -v4
	v_add_f32_e32 v5, 0, v84
	v_exp_f32_e32 v88, v6
	v_fma_f32 v6, v105, s63, -v4
	v_add_f32_e32 v5, v85, v5
	v_exp_f32_e32 v89, v6
	v_fma_f32 v6, v106, s63, -v4
	v_add_f32_e32 v5, v86, v5
	v_exp_f32_e32 v90, v6
	v_fma_f32 v6, v107, s63, -v4
	v_add_f32_e32 v5, v87, v5
	v_exp_f32_e32 v91, v6
	v_fma_f32 v6, v108, s63, -v4
	v_add_f32_e32 v5, v88, v5
	v_exp_f32_e32 v92, v6
	v_fma_f32 v6, v109, s63, -v4
	v_add_f32_e32 v5, v89, v5
	v_exp_f32_e32 v93, v6
	v_fma_f32 v6, v110, s63, -v4
	v_add_f32_e32 v5, v90, v5
	v_exp_f32_e32 v94, v6
	v_fma_f32 v6, v111, s63, -v4
	v_add_f32_e32 v5, v91, v5
	v_exp_f32_e32 v95, v6
	v_fma_f32 v6, v112, s63, -v4
	v_add_f32_e32 v5, v92, v5
	v_exp_f32_e32 v96, v6
	v_fma_f32 v6, v113, s63, -v4
	v_add_f32_e32 v5, v93, v5
	v_exp_f32_e32 v97, v6
	v_fma_f32 v6, v114, s63, -v4
	v_add_f32_e32 v5, v94, v5
	v_exp_f32_e32 v98, v6
	v_add_f32_e32 v5, v95, v5
	v_add_f32_e32 v5, v96, v5
	v_add_f32_e32 v5, v97, v5
	v_add_f32_e32 v6, v98, v5
	v_fma_f32 v5, v115, s63, -v4
	s_mov_b64 s[54:55], 0

.LBB0_2939:
	v_add_f32_e32 v14, v6, v6
	s_lshl_b32 s50, s59, 1
	v_fmac_f32_e32 v14, v82, v2
	s_add_i32 s50, s50, s86
	v_lshlrev_b32_e32 v2, 1, v186
	v_add3_u32 v2, s50, v198, v2
	v_add_u32_e32 v15, 0x4000, v2
	v_cvt_pk_bf16_f32 v6, v84, v85
	v_cvt_pk_bf16_f32 v7, v86, v87
	v_cvt_pk_bf16_f32 v8, v88, v89
	v_cvt_pk_bf16_f32 v9, v90, v91
	v_cvt_pk_bf16_f32 v92, v92, v93
	v_cvt_pk_bf16_f32 v93, v94, v95
	v_cvt_pk_bf16_f32 v94, v96, v97
	v_cvt_pk_bf16_f32 v95, v98, v5
	v_add_u32_e32 v16, 0x5000, v2
	v_add_u32_e32 v17, 0x6800, v2
	v_add_u32_e32 v2, 0x7800, v2
	v_mov_b32_e32 v82, v14
	ds_read2_b64 v[10:13], v15 offset0:128 offset1:130
	ds_read2_b64 v[248:251], v16 offset0:192 offset1:194
	ds_read2_b64 v[252:255], v17 offset1:2
	ds_read2_b64 v[84:87], v2 offset0:64 offset1:66
	ds_read2_b64 v[88:91], v15 offset0:132 offset1:134
	s_waitcnt lgkmcnt(4)
	v_mfma_f32_32x32x16_bf16 v[66:81], v[10:13], v[6:9], v[66:81]
	ds_read2_b64 v[10:13], v16 offset0:196 offset1:198
	s_waitcnt lgkmcnt(4)
	v_mfma_f32_32x32x16_bf16 v[50:65], v[248:251], v[6:9], v[50:65]
	ds_read2_b64 v[248:251], v17 offset0:4 offset1:6
	s_waitcnt lgkmcnt(4)
	v_mfma_f32_32x32x16_bf16 v[34:49], v[252:255], v[6:9], v[34:49]
	ds_read2_b64 v[252:255], v2 offset0:68 offset1:70
	s_waitcnt lgkmcnt(4)
	v_mfma_f32_32x32x16_bf16 v[18:33], v[84:87], v[6:9], v[18:33]
	s_waitcnt lgkmcnt(3)
	v_mfma_f32_32x32x16_bf16 v[66:81], v[88:91], v[92:95], v[66:81]
	s_waitcnt lgkmcnt(2)
	v_mfma_f32_32x32x16_bf16 v[50:65], v[10:13], v[92:95], v[50:65]
	s_waitcnt lgkmcnt(1)
	v_mfma_f32_32x32x16_bf16 v[34:49], v[248:251], v[92:95], v[34:49]
	s_waitcnt lgkmcnt(0)
	v_mfma_f32_32x32x16_bf16 v[18:33], v[252:255], v[92:95], v[18:33]
	s_andn2_b64 vcc, exec, s[48:49]
	s_cbranch_vccz .LBB0_2941
	s_branch .LBB0_2942
